# xo-GEMM epilogue: the second residual load of each row group issued together with the first, one wait per group
# baseline (speedup 1.0000x reference)
.LBB0_1950:
	v_lshl_add_u32 v148, s4, 8, v1
	s_lshl_b32 s28, s26, 8
	v_ashrrev_i32_e32 v149, 31, v148
	s_ashr_i32 s29, s28, 31
	v_lshlrev_b64 v[150:151], 11, v[148:149]
	v_lshl_add_u64 v[150:151], v[150:151], 0, s[28:29]
	v_readlane_b32 s48, v236, 24
	v_or_b32_e32 v152, v150, v138
	v_mov_b32_e32 v153, v151
	v_readlane_b32 s49, v236, 25
	v_cndmask_b32_e64 v162, 0, 1, s[16:17]
	v_cmp_ne_u32_e64 s[4:5], 1, v162
	v_lshl_add_u64 v[158:159], v[152:153], 1, s[48:49]
	global_load_dwordx4 v[158:161], v[158:159], off
	v_lshl_add_u64 v[170:171], v[150:151], 0, v[138:139]
	v_lshl_add_u64 v[170:171], v[170:171], 1, s[48:49]
	global_load_dwordx4 v[166:169], v[170:171], off offset:256
	s_andn2_b64 vcc, exec, s[16:17]
	v_readlane_b32 s50, v236, 26
	v_readlane_b32 s51, v236, 27
	v_readlane_b32 s52, v236, 28
	v_readlane_b32 s53, v236, 29
	v_readlane_b32 s54, v236, 30
	v_readlane_b32 s55, v236, 31
	s_waitcnt vmcnt(0)
	v_lshlrev_b32_e32 v162, 16, v158
	v_and_b32_e32 v163, 0xffff0000, v158
	v_lshlrev_b32_e32 v158, 16, v159
	v_and_b32_e32 v159, 0xffff0000, v159
	v_lshlrev_b32_e32 v164, 16, v160
	v_and_b32_e32 v165, 0xffff0000, v160
	v_lshlrev_b32_e32 v160, 16, v161
	v_and_b32_e32 v161, 0xffff0000, v161
	v_pk_add_f32 v[128:129], v[128:129], v[158:159]
	v_pk_add_f32 v[126:127], v[126:127], v[162:163]
	v_pk_add_f32 v[124:125], v[124:125], v[160:161]
	v_pk_add_f32 v[122:123], v[122:123], v[164:165]
	s_cbranch_vccnz .LBB0_1952
	v_lshl_add_u64 v[152:153], v[152:153], 1, s[58:59]
	v_cvt_pk_bf16_f32 v158, v126, v127
	v_cvt_pk_bf16_f32 v159, v128, v129
	v_cvt_pk_bf16_f32 v160, v122, v123
	v_cvt_pk_bf16_f32 v161, v124, v125
	global_store_dwordx4 v[152:153], v[158:161], off
.LBB0_1952:
	v_readlane_b32 s48, v236, 24
	v_lshl_add_u64 v[150:151], v[150:151], 0, v[138:139]
	v_readlane_b32 s49, v236, 25
	s_and_b64 vcc, exec, s[4:5]
	v_readlane_b32 s50, v236, 26
	v_readlane_b32 s51, v236, 27
	v_readlane_b32 s52, v236, 28
	v_readlane_b32 s53, v236, 29
	v_readlane_b32 s54, v236, 30
	v_readlane_b32 s55, v236, 31
	v_lshlrev_b32_e32 v152, 16, v166
	v_and_b32_e32 v153, 0xffff0000, v166
	v_lshlrev_b32_e32 v158, 16, v167
	v_and_b32_e32 v159, 0xffff0000, v167
	v_lshlrev_b32_e32 v162, 16, v168
	v_and_b32_e32 v163, 0xffff0000, v168
	v_lshlrev_b32_e32 v160, 16, v169
	v_and_b32_e32 v161, 0xffff0000, v169
	v_pk_add_f32 v[120:121], v[120:121], v[158:159]
	v_pk_add_f32 v[118:119], v[118:119], v[152:153]
	v_pk_add_f32 v[116:117], v[116:117], v[160:161]
	v_pk_add_f32 v[114:115], v[114:115], v[162:163]
	s_cbranch_vccnz .LBB0_1954
	v_lshl_add_u64 v[150:151], v[150:151], 1, s[58:59]
	v_cvt_pk_bf16_f32 v158, v118, v119
	v_cvt_pk_bf16_f32 v159, v120, v121
	v_cvt_pk_bf16_f32 v160, v114, v115
	v_cvt_pk_bf16_f32 v161, v116, v117
	global_store_dwordx4 v[150:151], v[158:161], off offset:256

.LBB0_1956:
	s_or_b64 exec, exec, s[30:31]
	v_or_b32_e32 v114, 16, v148
	v_ashrrev_i32_e32 v115, 31, v114
	v_lshlrev_b64 v[116:117], 11, v[114:115]
	v_lshl_add_u64 v[116:117], v[116:117], 0, s[28:29]
	v_readlane_b32 s48, v236, 24
	v_or_b32_e32 v118, v116, v138
	v_mov_b32_e32 v119, v117
	v_readlane_b32 s49, v236, 25
	s_and_b64 vcc, exec, s[4:5]
	v_readlane_b32 s50, v236, 26
	v_lshl_add_u64 v[120:121], v[118:119], 1, s[48:49]
	global_load_dwordx4 v[120:123], v[120:121], off
	v_lshl_add_u64 v[170:171], v[116:117], 0, v[138:139]
	v_lshl_add_u64 v[170:171], v[170:171], 1, s[48:49]
	global_load_dwordx4 v[166:169], v[170:171], off offset:256
	v_readlane_b32 s51, v236, 27
	v_readlane_b32 s52, v236, 28
	v_readlane_b32 s53, v236, 29
	v_readlane_b32 s54, v236, 30
	v_readlane_b32 s55, v236, 31
	s_waitcnt vmcnt(0)
	v_lshlrev_b32_e32 v124, 16, v120
	v_and_b32_e32 v125, 0xffff0000, v120
	v_lshlrev_b32_e32 v120, 16, v121
	v_and_b32_e32 v121, 0xffff0000, v121
	v_lshlrev_b32_e32 v126, 16, v122
	v_and_b32_e32 v127, 0xffff0000, v122
	v_lshlrev_b32_e32 v122, 16, v123
	v_and_b32_e32 v123, 0xffff0000, v123
	v_pk_add_f32 v[112:113], v[112:113], v[120:121]
	v_pk_add_f32 v[110:111], v[110:111], v[124:125]
	v_pk_add_f32 v[108:109], v[108:109], v[122:123]
	v_pk_add_f32 v[106:107], v[106:107], v[126:127]
	s_cbranch_vccnz .LBB0_1958
	v_lshl_add_u64 v[118:119], v[118:119], 1, s[58:59]
	v_cvt_pk_bf16_f32 v120, v110, v111
	v_cvt_pk_bf16_f32 v121, v112, v113
	v_cvt_pk_bf16_f32 v122, v106, v107
	v_cvt_pk_bf16_f32 v123, v108, v109
	global_store_dwordx4 v[118:119], v[120:123], off
.LBB0_1958:
	v_readlane_b32 s48, v236, 24
	v_lshl_add_u64 v[116:117], v[116:117], 0, v[138:139]
	v_readlane_b32 s49, v236, 25
	s_and_b64 vcc, exec, s[4:5]
	v_readlane_b32 s50, v236, 26
	v_readlane_b32 s51, v236, 27
	v_readlane_b32 s52, v236, 28
	v_readlane_b32 s53, v236, 29
	v_readlane_b32 s54, v236, 30
	v_readlane_b32 s55, v236, 31
	v_lshlrev_b32_e32 v122, 16, v166
	v_and_b32_e32 v123, 0xffff0000, v166
	v_lshlrev_b32_e32 v118, 16, v167
	v_and_b32_e32 v119, 0xffff0000, v167
	v_lshlrev_b32_e32 v124, 16, v168
	v_and_b32_e32 v125, 0xffff0000, v168
	v_lshlrev_b32_e32 v120, 16, v169
	v_and_b32_e32 v121, 0xffff0000, v169
	v_pk_add_f32 v[104:105], v[104:105], v[118:119]
	v_pk_add_f32 v[102:103], v[102:103], v[122:123]
	v_pk_add_f32 v[100:101], v[100:101], v[120:121]
	v_pk_add_f32 v[98:99], v[98:99], v[124:125]
	s_cbranch_vccnz .LBB0_1960
	v_lshl_add_u64 v[116:117], v[116:117], 1, s[58:59]
	v_cvt_pk_bf16_f32 v118, v102, v103
	v_cvt_pk_bf16_f32 v119, v104, v105
	v_cvt_pk_bf16_f32 v120, v98, v99
	v_cvt_pk_bf16_f32 v121, v100, v101
	global_store_dwordx4 v[116:117], v[118:121], off offset:256

.LBB0_1962:
	s_or_b64 exec, exec, s[30:31]
	v_or_b32_e32 v98, 32, v148
	v_ashrrev_i32_e32 v99, 31, v98
	v_lshlrev_b64 v[100:101], 11, v[98:99]
	v_lshl_add_u64 v[100:101], v[100:101], 0, s[28:29]
	v_readlane_b32 s48, v236, 24
	v_or_b32_e32 v102, v100, v138
	v_mov_b32_e32 v103, v101
	v_readlane_b32 s49, v236, 25
	s_and_b64 vcc, exec, s[4:5]
	v_readlane_b32 s50, v236, 26
	v_lshl_add_u64 v[104:105], v[102:103], 1, s[48:49]
	global_load_dwordx4 v[104:107], v[104:105], off
	v_lshl_add_u64 v[170:171], v[100:101], 0, v[138:139]
	v_lshl_add_u64 v[170:171], v[170:171], 1, s[48:49]
	global_load_dwordx4 v[166:169], v[170:171], off offset:256
	v_readlane_b32 s51, v236, 27
	v_readlane_b32 s52, v236, 28
	v_readlane_b32 s53, v236, 29
	v_readlane_b32 s54, v236, 30
	v_readlane_b32 s55, v236, 31
	s_waitcnt vmcnt(0)
	v_lshlrev_b32_e32 v108, 16, v104
	v_and_b32_e32 v109, 0xffff0000, v104
	v_lshlrev_b32_e32 v104, 16, v105
	v_and_b32_e32 v105, 0xffff0000, v105
	v_lshlrev_b32_e32 v110, 16, v106
	v_and_b32_e32 v111, 0xffff0000, v106
	v_lshlrev_b32_e32 v106, 16, v107
	v_and_b32_e32 v107, 0xffff0000, v107
	v_pk_add_f32 v[96:97], v[96:97], v[104:105]
	v_pk_add_f32 v[94:95], v[94:95], v[108:109]
	v_pk_add_f32 v[92:93], v[92:93], v[106:107]
	v_pk_add_f32 v[90:91], v[90:91], v[110:111]
	s_cbranch_vccnz .LBB0_1964
	v_lshl_add_u64 v[102:103], v[102:103], 1, s[58:59]
	v_cvt_pk_bf16_f32 v104, v94, v95
	v_cvt_pk_bf16_f32 v105, v96, v97
	v_cvt_pk_bf16_f32 v106, v90, v91
	v_cvt_pk_bf16_f32 v107, v92, v93
	global_store_dwordx4 v[102:103], v[104:107], off
.LBB0_1964:
	v_readlane_b32 s48, v236, 24
	v_lshl_add_u64 v[100:101], v[100:101], 0, v[138:139]
	v_readlane_b32 s49, v236, 25
	s_and_b64 vcc, exec, s[4:5]
	v_readlane_b32 s50, v236, 26
	v_readlane_b32 s51, v236, 27
	v_readlane_b32 s52, v236, 28
	v_readlane_b32 s53, v236, 29
	v_readlane_b32 s54, v236, 30
	v_readlane_b32 s55, v236, 31
	v_lshlrev_b32_e32 v106, 16, v166
	v_and_b32_e32 v107, 0xffff0000, v166
	v_lshlrev_b32_e32 v102, 16, v167
	v_and_b32_e32 v103, 0xffff0000, v167
	v_lshlrev_b32_e32 v108, 16, v168
	v_and_b32_e32 v109, 0xffff0000, v168
	v_lshlrev_b32_e32 v104, 16, v169
	v_and_b32_e32 v105, 0xffff0000, v169
	v_pk_add_f32 v[88:89], v[88:89], v[102:103]
	v_pk_add_f32 v[86:87], v[86:87], v[106:107]
	v_pk_add_f32 v[84:85], v[84:85], v[104:105]
	v_pk_add_f32 v[82:83], v[82:83], v[108:109]
	s_cbranch_vccnz .LBB0_1966
	v_lshl_add_u64 v[100:101], v[100:101], 1, s[58:59]
	v_cvt_pk_bf16_f32 v102, v86, v87
	v_cvt_pk_bf16_f32 v103, v88, v89
	v_cvt_pk_bf16_f32 v104, v82, v83
	v_cvt_pk_bf16_f32 v105, v84, v85
	global_store_dwordx4 v[100:101], v[102:105], off offset:256

.LBB0_1968:
	s_or_b64 exec, exec, s[30:31]
	v_or_b32_e32 v82, 48, v148
	v_ashrrev_i32_e32 v83, 31, v82
	v_lshlrev_b64 v[84:85], 11, v[82:83]
	v_lshl_add_u64 v[84:85], v[84:85], 0, s[28:29]
	v_readlane_b32 s48, v236, 24
	v_or_b32_e32 v86, v84, v138
	v_mov_b32_e32 v87, v85
	v_readlane_b32 s49, v236, 25
	s_and_b64 vcc, exec, s[4:5]
	v_readlane_b32 s50, v236, 26
	v_lshl_add_u64 v[88:89], v[86:87], 1, s[48:49]
	global_load_dwordx4 v[88:91], v[88:89], off
	v_lshl_add_u64 v[170:171], v[84:85], 0, v[138:139]
	v_lshl_add_u64 v[170:171], v[170:171], 1, s[48:49]
	global_load_dwordx4 v[166:169], v[170:171], off offset:256
	v_readlane_b32 s51, v236, 27
	v_readlane_b32 s52, v236, 28
	v_readlane_b32 s53, v236, 29
	v_readlane_b32 s54, v236, 30
	v_readlane_b32 s55, v236, 31
	s_waitcnt vmcnt(0)
	v_lshlrev_b32_e32 v92, 16, v88
	v_and_b32_e32 v93, 0xffff0000, v88
	v_lshlrev_b32_e32 v88, 16, v89
	v_and_b32_e32 v89, 0xffff0000, v89
	v_lshlrev_b32_e32 v94, 16, v90
	v_and_b32_e32 v95, 0xffff0000, v90
	v_lshlrev_b32_e32 v90, 16, v91
	v_and_b32_e32 v91, 0xffff0000, v91
	v_pk_add_f32 v[80:81], v[80:81], v[88:89]
	v_pk_add_f32 v[78:79], v[78:79], v[92:93]
	v_pk_add_f32 v[76:77], v[76:77], v[90:91]
	v_pk_add_f32 v[74:75], v[74:75], v[94:95]
	s_cbranch_vccnz .LBB0_1970
	v_lshl_add_u64 v[86:87], v[86:87], 1, s[58:59]
	v_cvt_pk_bf16_f32 v88, v78, v79
	v_cvt_pk_bf16_f32 v89, v80, v81
	v_cvt_pk_bf16_f32 v90, v74, v75
	v_cvt_pk_bf16_f32 v91, v76, v77
	global_store_dwordx4 v[86:87], v[88:91], off
.LBB0_1970:
	v_readlane_b32 s48, v236, 24
	v_lshl_add_u64 v[84:85], v[84:85], 0, v[138:139]
	v_readlane_b32 s49, v236, 25
	s_and_b64 vcc, exec, s[4:5]
	v_readlane_b32 s50, v236, 26
	v_readlane_b32 s51, v236, 27
	v_readlane_b32 s52, v236, 28
	v_readlane_b32 s53, v236, 29
	v_readlane_b32 s54, v236, 30
	v_readlane_b32 s55, v236, 31
	v_lshlrev_b32_e32 v90, 16, v166
	v_and_b32_e32 v91, 0xffff0000, v166
	v_lshlrev_b32_e32 v86, 16, v167
	v_and_b32_e32 v87, 0xffff0000, v167
	v_lshlrev_b32_e32 v92, 16, v168
	v_and_b32_e32 v93, 0xffff0000, v168
	v_lshlrev_b32_e32 v88, 16, v169
	v_and_b32_e32 v89, 0xffff0000, v169
	v_pk_add_f32 v[72:73], v[72:73], v[86:87]
	v_pk_add_f32 v[70:71], v[70:71], v[90:91]
	v_pk_add_f32 v[68:69], v[68:69], v[88:89]
	v_pk_add_f32 v[66:67], v[66:67], v[92:93]
	s_cbranch_vccnz .LBB0_1972
	v_lshl_add_u64 v[84:85], v[84:85], 1, s[58:59]
	v_cvt_pk_bf16_f32 v86, v70, v71
	v_cvt_pk_bf16_f32 v87, v72, v73
	v_cvt_pk_bf16_f32 v88, v66, v67
	v_cvt_pk_bf16_f32 v89, v68, v69
	global_store_dwordx4 v[84:85], v[86:89], off offset:256

.LBB0_1974:
	s_or_b64 exec, exec, s[30:31]
	v_add_u32_e32 v66, 0x80, v148
	v_ashrrev_i32_e32 v67, 31, v66
	v_lshlrev_b64 v[68:69], 11, v[66:67]
	v_lshl_add_u64 v[68:69], v[68:69], 0, s[28:29]
	v_readlane_b32 s48, v236, 24
	v_or_b32_e32 v70, v68, v138
	v_mov_b32_e32 v71, v69
	v_readlane_b32 s49, v236, 25
	s_and_b64 vcc, exec, s[4:5]
	v_readlane_b32 s50, v236, 26
	v_lshl_add_u64 v[72:73], v[70:71], 1, s[48:49]
	global_load_dwordx4 v[72:75], v[72:73], off
	v_lshl_add_u64 v[170:171], v[68:69], 0, v[138:139]
	v_lshl_add_u64 v[170:171], v[170:171], 1, s[48:49]
	global_load_dwordx4 v[166:169], v[170:171], off offset:256
	v_readlane_b32 s51, v236, 27
	v_readlane_b32 s52, v236, 28
	v_readlane_b32 s53, v236, 29
	v_readlane_b32 s54, v236, 30
	v_readlane_b32 s55, v236, 31
	s_waitcnt vmcnt(0)
	v_lshlrev_b32_e32 v76, 16, v72
	v_and_b32_e32 v77, 0xffff0000, v72
	v_lshlrev_b32_e32 v72, 16, v73
	v_and_b32_e32 v73, 0xffff0000, v73
	v_lshlrev_b32_e32 v78, 16, v74
	v_and_b32_e32 v79, 0xffff0000, v74
	v_lshlrev_b32_e32 v74, 16, v75
	v_and_b32_e32 v75, 0xffff0000, v75
	v_pk_add_f32 v[64:65], v[64:65], v[72:73]
	v_pk_add_f32 v[62:63], v[62:63], v[76:77]
	v_pk_add_f32 v[60:61], v[60:61], v[74:75]
	v_pk_add_f32 v[58:59], v[58:59], v[78:79]
	s_cbranch_vccnz .LBB0_1976
	v_lshl_add_u64 v[70:71], v[70:71], 1, s[58:59]
	v_cvt_pk_bf16_f32 v72, v62, v63
	v_cvt_pk_bf16_f32 v73, v64, v65
	v_cvt_pk_bf16_f32 v74, v58, v59
	v_cvt_pk_bf16_f32 v75, v60, v61
	global_store_dwordx4 v[70:71], v[72:75], off
.LBB0_1976:
	v_readlane_b32 s48, v236, 24
	v_lshl_add_u64 v[68:69], v[68:69], 0, v[138:139]
	v_readlane_b32 s49, v236, 25
	s_and_b64 vcc, exec, s[4:5]
	v_readlane_b32 s50, v236, 26
	v_readlane_b32 s51, v236, 27
	v_readlane_b32 s52, v236, 28
	v_readlane_b32 s53, v236, 29
	v_readlane_b32 s54, v236, 30
	v_readlane_b32 s55, v236, 31
	v_lshlrev_b32_e32 v74, 16, v166
	v_and_b32_e32 v75, 0xffff0000, v166
	v_lshlrev_b32_e32 v70, 16, v167
	v_and_b32_e32 v71, 0xffff0000, v167
	v_lshlrev_b32_e32 v76, 16, v168
	v_and_b32_e32 v77, 0xffff0000, v168
	v_lshlrev_b32_e32 v72, 16, v169
	v_and_b32_e32 v73, 0xffff0000, v169
	v_pk_add_f32 v[56:57], v[56:57], v[70:71]
	v_pk_add_f32 v[54:55], v[54:55], v[74:75]
	v_pk_add_f32 v[52:53], v[52:53], v[72:73]
	v_pk_add_f32 v[50:51], v[50:51], v[76:77]
	s_cbranch_vccnz .LBB0_1978
	v_lshl_add_u64 v[68:69], v[68:69], 1, s[58:59]
	v_cvt_pk_bf16_f32 v70, v54, v55
	v_cvt_pk_bf16_f32 v71, v56, v57
	v_cvt_pk_bf16_f32 v72, v50, v51
	v_cvt_pk_bf16_f32 v73, v52, v53
	global_store_dwordx4 v[68:69], v[70:73], off offset:256

.LBB0_1980:
	s_or_b64 exec, exec, s[30:31]
	v_add_u32_e32 v50, 0x90, v148
	v_ashrrev_i32_e32 v51, 31, v50
	v_lshlrev_b64 v[52:53], 11, v[50:51]
	v_lshl_add_u64 v[52:53], v[52:53], 0, s[28:29]
	v_readlane_b32 s48, v236, 24
	v_or_b32_e32 v54, v52, v138
	v_mov_b32_e32 v55, v53
	v_readlane_b32 s49, v236, 25
	s_and_b64 vcc, exec, s[4:5]
	v_readlane_b32 s50, v236, 26
	v_lshl_add_u64 v[56:57], v[54:55], 1, s[48:49]
	global_load_dwordx4 v[56:59], v[56:57], off
	v_lshl_add_u64 v[170:171], v[52:53], 0, v[138:139]
	v_lshl_add_u64 v[170:171], v[170:171], 1, s[48:49]
	global_load_dwordx4 v[166:169], v[170:171], off offset:256
	v_readlane_b32 s51, v236, 27
	v_readlane_b32 s52, v236, 28
	v_readlane_b32 s53, v236, 29
	v_readlane_b32 s54, v236, 30
	v_readlane_b32 s55, v236, 31
	s_waitcnt vmcnt(0)
	v_lshlrev_b32_e32 v60, 16, v56
	v_and_b32_e32 v61, 0xffff0000, v56
	v_lshlrev_b32_e32 v56, 16, v57
	v_and_b32_e32 v57, 0xffff0000, v57
	v_lshlrev_b32_e32 v62, 16, v58
	v_and_b32_e32 v63, 0xffff0000, v58
	v_lshlrev_b32_e32 v58, 16, v59
	v_and_b32_e32 v59, 0xffff0000, v59
	v_pk_add_f32 v[48:49], v[48:49], v[56:57]
	v_pk_add_f32 v[46:47], v[46:47], v[60:61]
	v_pk_add_f32 v[44:45], v[44:45], v[58:59]
	v_pk_add_f32 v[42:43], v[42:43], v[62:63]
	s_cbranch_vccnz .LBB0_1982
	v_lshl_add_u64 v[54:55], v[54:55], 1, s[58:59]
	v_cvt_pk_bf16_f32 v56, v46, v47
	v_cvt_pk_bf16_f32 v57, v48, v49
	v_cvt_pk_bf16_f32 v58, v42, v43
	v_cvt_pk_bf16_f32 v59, v44, v45
	global_store_dwordx4 v[54:55], v[56:59], off
.LBB0_1982:
	v_readlane_b32 s48, v236, 24
	v_lshl_add_u64 v[52:53], v[52:53], 0, v[138:139]
	v_readlane_b32 s49, v236, 25
	s_and_b64 vcc, exec, s[4:5]
	v_readlane_b32 s50, v236, 26
	v_readlane_b32 s51, v236, 27
	v_readlane_b32 s52, v236, 28
	v_readlane_b32 s53, v236, 29
	v_readlane_b32 s54, v236, 30
	v_readlane_b32 s55, v236, 31
	v_lshlrev_b32_e32 v58, 16, v166
	v_and_b32_e32 v59, 0xffff0000, v166
	v_lshlrev_b32_e32 v54, 16, v167
	v_and_b32_e32 v55, 0xffff0000, v167
	v_lshlrev_b32_e32 v60, 16, v168
	v_and_b32_e32 v61, 0xffff0000, v168
	v_lshlrev_b32_e32 v56, 16, v169
	v_and_b32_e32 v57, 0xffff0000, v169
	v_pk_add_f32 v[40:41], v[40:41], v[54:55]
	v_pk_add_f32 v[38:39], v[38:39], v[58:59]
	v_pk_add_f32 v[36:37], v[36:37], v[56:57]
	v_pk_add_f32 v[34:35], v[34:35], v[60:61]
	s_cbranch_vccnz .LBB0_1984
	v_lshl_add_u64 v[52:53], v[52:53], 1, s[58:59]
	v_cvt_pk_bf16_f32 v54, v38, v39
	v_cvt_pk_bf16_f32 v55, v40, v41
	v_cvt_pk_bf16_f32 v56, v34, v35
	v_cvt_pk_bf16_f32 v57, v36, v37
	global_store_dwordx4 v[52:53], v[54:57], off offset:256

.LBB0_1986:
	s_or_b64 exec, exec, s[30:31]
	v_add_u32_e32 v34, 0xa0, v148
	v_ashrrev_i32_e32 v35, 31, v34
	v_lshlrev_b64 v[36:37], 11, v[34:35]
	v_lshl_add_u64 v[36:37], v[36:37], 0, s[28:29]
	v_readlane_b32 s48, v236, 24
	v_or_b32_e32 v38, v36, v138
	v_mov_b32_e32 v39, v37
	v_readlane_b32 s49, v236, 25
	s_and_b64 vcc, exec, s[4:5]
	v_readlane_b32 s50, v236, 26
	v_lshl_add_u64 v[40:41], v[38:39], 1, s[48:49]
	global_load_dwordx4 v[40:43], v[40:41], off
	v_lshl_add_u64 v[170:171], v[36:37], 0, v[138:139]
	v_lshl_add_u64 v[170:171], v[170:171], 1, s[48:49]
	global_load_dwordx4 v[166:169], v[170:171], off offset:256
	v_readlane_b32 s51, v236, 27
	v_readlane_b32 s52, v236, 28
	v_readlane_b32 s53, v236, 29
	v_readlane_b32 s54, v236, 30
	v_readlane_b32 s55, v236, 31
	s_waitcnt vmcnt(0)
	v_lshlrev_b32_e32 v44, 16, v40
	v_and_b32_e32 v45, 0xffff0000, v40
	v_lshlrev_b32_e32 v40, 16, v41
	v_and_b32_e32 v41, 0xffff0000, v41
	v_lshlrev_b32_e32 v46, 16, v42
	v_and_b32_e32 v47, 0xffff0000, v42
	v_lshlrev_b32_e32 v42, 16, v43
	v_and_b32_e32 v43, 0xffff0000, v43
	v_pk_add_f32 v[32:33], v[32:33], v[40:41]
	v_pk_add_f32 v[30:31], v[30:31], v[44:45]
	v_pk_add_f32 v[28:29], v[28:29], v[42:43]
	v_pk_add_f32 v[26:27], v[26:27], v[46:47]
	s_cbranch_vccnz .LBB0_1988
	v_lshl_add_u64 v[38:39], v[38:39], 1, s[58:59]
	v_cvt_pk_bf16_f32 v40, v30, v31
	v_cvt_pk_bf16_f32 v41, v32, v33
	v_cvt_pk_bf16_f32 v42, v26, v27
	v_cvt_pk_bf16_f32 v43, v28, v29
	global_store_dwordx4 v[38:39], v[40:43], off
.LBB0_1988:
	v_readlane_b32 s48, v236, 24
	v_lshl_add_u64 v[36:37], v[36:37], 0, v[138:139]
	v_readlane_b32 s49, v236, 25
	s_and_b64 vcc, exec, s[4:5]
	v_readlane_b32 s50, v236, 26
	v_readlane_b32 s51, v236, 27
	v_readlane_b32 s52, v236, 28
	v_readlane_b32 s53, v236, 29
	v_readlane_b32 s54, v236, 30
	v_readlane_b32 s55, v236, 31
	v_lshlrev_b32_e32 v42, 16, v166
	v_and_b32_e32 v43, 0xffff0000, v166
	v_lshlrev_b32_e32 v38, 16, v167
	v_and_b32_e32 v39, 0xffff0000, v167
	v_lshlrev_b32_e32 v44, 16, v168
	v_and_b32_e32 v45, 0xffff0000, v168
	v_lshlrev_b32_e32 v40, 16, v169
	v_and_b32_e32 v41, 0xffff0000, v169
	v_pk_add_f32 v[24:25], v[24:25], v[38:39]
	v_pk_add_f32 v[22:23], v[22:23], v[42:43]
	v_pk_add_f32 v[20:21], v[20:21], v[40:41]
	v_pk_add_f32 v[18:19], v[18:19], v[44:45]
	s_cbranch_vccnz .LBB0_1990
	v_lshl_add_u64 v[36:37], v[36:37], 1, s[58:59]
	v_cvt_pk_bf16_f32 v38, v22, v23
	v_cvt_pk_bf16_f32 v39, v24, v25
	v_cvt_pk_bf16_f32 v40, v18, v19
	v_cvt_pk_bf16_f32 v41, v20, v21
	global_store_dwordx4 v[36:37], v[38:41], off offset:256

.LBB0_1992:
	s_or_b64 exec, exec, s[30:31]
	v_add_u32_e32 v18, 0xb0, v148
	v_ashrrev_i32_e32 v19, 31, v18
	v_lshlrev_b64 v[20:21], 11, v[18:19]
	v_lshl_add_u64 v[20:21], v[20:21], 0, s[28:29]
	v_readlane_b32 s48, v236, 24
	v_or_b32_e32 v22, v20, v138
	v_mov_b32_e32 v23, v21
	v_readlane_b32 s49, v236, 25
	s_and_b64 vcc, exec, s[4:5]
	v_readlane_b32 s50, v236, 26
	v_lshl_add_u64 v[24:25], v[22:23], 1, s[48:49]
	global_load_dwordx4 v[24:27], v[24:25], off
	v_lshl_add_u64 v[170:171], v[20:21], 0, v[138:139]
	v_lshl_add_u64 v[170:171], v[170:171], 1, s[48:49]
	global_load_dwordx4 v[166:169], v[170:171], off offset:256
	v_readlane_b32 s51, v236, 27
	v_readlane_b32 s52, v236, 28
	v_readlane_b32 s53, v236, 29
	v_readlane_b32 s54, v236, 30
	v_readlane_b32 s55, v236, 31
	s_waitcnt vmcnt(0)
	v_lshlrev_b32_e32 v28, 16, v24
	v_and_b32_e32 v29, 0xffff0000, v24
	v_lshlrev_b32_e32 v24, 16, v25
	v_and_b32_e32 v25, 0xffff0000, v25
	v_lshlrev_b32_e32 v30, 16, v26
	v_and_b32_e32 v31, 0xffff0000, v26
	v_lshlrev_b32_e32 v26, 16, v27
	v_and_b32_e32 v27, 0xffff0000, v27
	v_pk_add_f32 v[16:17], v[16:17], v[24:25]
	v_pk_add_f32 v[14:15], v[14:15], v[28:29]
	v_pk_add_f32 v[12:13], v[12:13], v[26:27]
	v_pk_add_f32 v[10:11], v[10:11], v[30:31]
	s_cbranch_vccnz .LBB0_1994
	v_lshl_add_u64 v[22:23], v[22:23], 1, s[58:59]
	v_cvt_pk_bf16_f32 v24, v14, v15
	v_cvt_pk_bf16_f32 v25, v16, v17
	v_cvt_pk_bf16_f32 v26, v10, v11
	v_cvt_pk_bf16_f32 v27, v12, v13
	global_store_dwordx4 v[22:23], v[24:27], off
.LBB0_1994:
	v_readlane_b32 s48, v236, 24
	v_lshl_add_u64 v[20:21], v[20:21], 0, v[138:139]
	v_readlane_b32 s49, v236, 25
	s_and_b64 vcc, exec, s[4:5]
	v_readlane_b32 s50, v236, 26
	v_readlane_b32 s51, v236, 27
	v_readlane_b32 s52, v236, 28
	v_readlane_b32 s53, v236, 29
	v_readlane_b32 s54, v236, 30
	v_readlane_b32 s55, v236, 31
	v_lshlrev_b32_e32 v26, 16, v166
	v_and_b32_e32 v27, 0xffff0000, v166
	v_lshlrev_b32_e32 v22, 16, v167
	v_and_b32_e32 v23, 0xffff0000, v167
	v_lshlrev_b32_e32 v28, 16, v168
	v_and_b32_e32 v29, 0xffff0000, v168
	v_lshlrev_b32_e32 v24, 16, v169
	v_and_b32_e32 v25, 0xffff0000, v169
	v_pk_add_f32 v[8:9], v[8:9], v[22:23]
	v_pk_add_f32 v[6:7], v[6:7], v[26:27]
	v_pk_add_f32 v[4:5], v[4:5], v[24:25]
	v_pk_add_f32 v[2:3], v[2:3], v[28:29]
	s_cbranch_vccnz .LBB0_1996
	v_lshl_add_u64 v[20:21], v[20:21], 1, s[58:59]
	v_cvt_pk_bf16_f32 v22, v6, v7
	v_cvt_pk_bf16_f32 v23, v8, v9
	v_cvt_pk_bf16_f32 v24, v2, v3
	v_cvt_pk_bf16_f32 v25, v4, v5
	global_store_dwordx4 v[20:21], v[22:25], off offset:256
